# P4 RG gate epilogue: all twelve loads issued together before one counted wait (prologue de-serialisation); no other change
# speedup vs baseline: 1.0020x; 1.0020x over previous
.LBB0_640:
	s_and_b32 s75, s12, 1
	s_lshl_b32 s12, s12, 6
	s_and_b32 s12, s12, 0xffffff80
	v_mov_b32_e32 v130, v182
	v_mov_b32_e32 v131, v183
	s_or_b32 s12, s12, s63
	s_nop 0
	v_lshl_add_u32 v132, v131, 3, s12
	s_lshl_b32 s12, s75, 12
	s_waitcnt lgkmcnt(0)
	s_add_u32 s28, s10, s12
	s_addc_u32 s29, s11, 0
	s_ashr_i32 s25, s24, 31
	s_lshl_b64 s[24:25], s[24:25], 8
	v_ashrrev_i32_e32 v133, 31, v132
	s_add_u32 s24, s24, s62
	v_lshlrev_b64 v[134:135], 2, v[132:133]
	s_addc_u32 s25, s25, s67
	v_lshl_add_u64 v[136:137], s[28:29], 0, v[134:135]
	s_add_u32 s28, s8, s12
	s_addc_u32 s29, s9, 0
	global_load_dwordx4 v[142:145], v[136:137], off
	v_lshl_add_u64 v[134:135], s[28:29], 0, v[134:135]
	global_load_dwordx4 v[146:149], v[134:135], off
	v_ashrrev_i32_e32 v131, 31, v130
	v_lshlrev_b64 v[208:209], 1, v[132:133]
	v_lshl_add_u64 v[138:139], s[24:25], 0, v[130:131]
	v_lshl_add_u64 v[132:133], s[4:5], 0, v[208:209]
	v_lshlrev_b64 v[130:131], 11, v[138:139]
	v_lshl_add_u64 v[140:141], v[132:133], 0, v[130:131]
	global_load_dwordx4 v[204:207], v[140:141], off
	global_load_dwordx4 v[130:133], v[136:137], off offset:16
	s_nop 0
	global_load_dwordx4 v[134:137], v[134:135], off offset:16
	s_mul_i32 s12, s75, 0x8400
	v_lshl_add_u64 v[214:215], v[138:139], 0, s[12:13]
	v_add_co_u32_e32 v138, vcc, s65, v140
	s_nop 1
	v_addc_co_u32_e32 v139, vcc, 0, v141, vcc
	v_add_co_u32_e32 v150, vcc, s54, v140
	s_nop 1
	v_addc_co_u32_e32 v151, vcc, 0, v141, vcc
	v_add_co_u32_e32 v152, vcc, s64, v140
	s_nop 1
	v_addc_co_u32_e32 v153, vcc, 0, v141, vcc
	v_add_co_u32_e32 v154, vcc, s69, v140
	s_nop 1
	v_addc_co_u32_e32 v155, vcc, 0, v141, vcc
	v_add_co_u32_e32 v156, vcc, s70, v140
	s_nop 1
	v_addc_co_u32_e32 v157, vcc, 0, v141, vcc
	v_add_co_u32_e32 v216, vcc, s71, v140
	s_nop 1
	v_addc_co_u32_e32 v217, vcc, 0, v141, vcc
	v_add_co_u32_e32 v140, vcc, s72, v140
	s_nop 1
	v_addc_co_u32_e32 v141, vcc, 0, v141, vcc
	global_load_dwordx4 v[170:173], v[138:139], off
	global_load_dwordx4 v[166:169], v[150:151], off
	global_load_dwordx4 v[162:165], v[152:153], off
	global_load_dwordx4 v[158:161], v[154:155], off
	s_nop 0
	global_load_dwordx4 v[154:157], v[156:157], off
	s_nop 0
	global_load_dwordx4 v[150:153], v[216:217], off
	s_nop 0
	global_load_dwordx4 v[138:141], v[140:141], off
	s_waitcnt vmcnt(7)
	v_add_f32_e32 v123, v123, v143
	v_mul_f32_e32 v123, 0xbfb8aa3b, v123
	v_add_f32_e32 v127, v127, v147
	v_exp_f32_e32 v123, v123
	v_mul_f32_e32 v127, 0xbfb8aa3b, v127
	v_exp_f32_e32 v127, v127
	v_add_f32_e32 v122, v122, v142
	v_add_f32_e32 v124, v124, v144
	v_mul_f32_e32 v122, 0xbfb8aa3b, v122
	v_add_f32_e32 v126, v126, v146
	v_add_f32_e32 v128, v128, v148
	v_add_f32_e32 v129, v129, v149
	v_add_f32_e32 v123, 1.0, v123
	v_add_f32_e32 v125, v125, v145
	v_mul_f32_e32 v124, 0xbfb8aa3b, v124
	v_exp_f32_e32 v122, v122
	v_mul_f32_e32 v126, 0xbfb8aa3b, v126
	v_mul_f32_e32 v128, 0xbfb8aa3b, v128
	v_rcp_f32_e32 v211, v123
	v_add_f32_e32 v123, 1.0, v127
	v_mul_f32_e32 v127, 0xbfb8aa3b, v129
	v_mul_f32_e32 v125, 0xbfb8aa3b, v125
	v_add_f32_e32 v118, v118, v134
	v_add_f32_e32 v119, v119, v135
	v_exp_f32_e32 v124, v124
	v_exp_f32_e32 v126, v126
	v_exp_f32_e32 v128, v128
	v_exp_f32_e32 v127, v127
	v_exp_f32_e32 v125, v125
	v_mul_f32_e32 v118, 0xbfb8aa3b, v118
	v_mul_f32_e32 v119, 0xbfb8aa3b, v119
	v_exp_f32_e32 v118, v118
	v_exp_f32_e32 v119, v119
	v_add_f32_e32 v122, 1.0, v122
	v_add_f32_e32 v106, v106, v142
	v_add_f32_e32 v124, 1.0, v124
	v_rcp_f32_e32 v203, v122
	v_add_f32_e32 v122, 1.0, v126
	v_add_f32_e32 v126, 1.0, v128
	v_add_f32_e32 v127, 1.0, v127
	v_add_f32_e32 v125, 1.0, v125
	v_mul_f32_e32 v106, 0xbfb8aa3b, v106
	v_add_f32_e32 v111, v111, v147
	v_rcp_f32_e32 v122, v122
	v_rcp_f32_e32 v123, v123
	v_rcp_f32_e32 v126, v126
	v_rcp_f32_e32 v124, v124
	v_rcp_f32_e32 v127, v127
	v_rcp_f32_e32 v125, v125
	v_add_f32_e32 v118, 1.0, v118
	v_add_f32_e32 v119, 1.0, v119
	v_exp_f32_e32 v106, v106
	v_mul_f32_e32 v111, 0xbfb8aa3b, v111
	v_rcp_f32_e32 v118, v118
	v_rcp_f32_e32 v119, v119
	v_exp_f32_e32 v111, v111
	v_lshlrev_b32_e32 v128, 16, v204
	v_and_b32_e32 v129, 0xffff0000, v204
	v_lshlrev_b32_e32 v204, 16, v205
	v_and_b32_e32 v205, 0xffff0000, v205
	v_cvt_pk_bf16_f32 v122, v122, v123
	v_cvt_pk_bf16_f32 v123, v126, v127
	v_mul_f32_e32 v126, v203, v128
	v_mul_f32_e32 v127, v211, v129
	v_mul_f32_e32 v124, v124, v204
	v_mul_f32_e32 v125, v125, v205
	v_add_f32_e32 v106, 1.0, v106
	v_add_f32_e32 v107, v107, v143
	v_cvt_pk_bf16_f32 v126, v126, v127
	v_cvt_pk_bf16_f32 v127, v124, v125
	v_cvt_pk_bf16_f32 v124, v118, v119
	v_mul_f32_e32 v107, 0xbfb8aa3b, v107
	v_rcp_f32_e32 v118, v106
	v_add_f32_e32 v106, 1.0, v111
	v_add_f32_e32 v111, v112, v148
	v_exp_f32_e32 v107, v107
	v_mul_f32_e32 v111, 0xbfb8aa3b, v111
	v_exp_f32_e32 v111, v111
	v_add_f32_e32 v114, v114, v130
	v_add_f32_e32 v115, v115, v131
	v_mul_f32_e32 v114, 0xbfb8aa3b, v114
	v_mul_f32_e32 v115, 0xbfb8aa3b, v115
	v_add_f32_e32 v116, v116, v132
	v_add_f32_e32 v117, v117, v133
	v_add_f32_e32 v107, 1.0, v107
	v_exp_f32_e32 v114, v114
	v_exp_f32_e32 v115, v115
	v_mul_f32_e32 v116, 0xbfb8aa3b, v116
	v_mul_f32_e32 v117, 0xbfb8aa3b, v117
	v_add_f32_e32 v110, v110, v146
	v_rcp_f32_e32 v112, v107
	v_add_f32_e32 v107, 1.0, v111
	v_add_f32_e32 v111, v113, v149
	v_exp_f32_e32 v116, v116
	v_exp_f32_e32 v117, v117
	v_mul_f32_e32 v110, 0xbfb8aa3b, v110
	v_mul_f32_e32 v111, 0xbfb8aa3b, v111
	v_add_f32_e32 v98, v98, v130
	v_add_f32_e32 v99, v99, v131
	v_add_f32_e32 v120, v120, v136
	v_add_f32_e32 v121, v121, v137
	v_exp_f32_e32 v110, v110
	v_exp_f32_e32 v111, v111
	v_mul_f32_e32 v98, 0xbfb8aa3b, v98
	v_mul_f32_e32 v99, 0xbfb8aa3b, v99
	v_add_f32_e32 v100, v100, v132
	v_add_f32_e32 v101, v101, v133
	v_mul_f32_e32 v120, 0xbfb8aa3b, v120
	v_mul_f32_e32 v121, 0xbfb8aa3b, v121
	v_add_f32_e32 v108, v108, v144
	v_add_f32_e32 v109, v109, v145
	v_exp_f32_e32 v98, v98
	v_exp_f32_e32 v99, v99
	v_mul_f32_e32 v100, 0xbfb8aa3b, v100
	v_mul_f32_e32 v101, 0xbfb8aa3b, v101
	v_add_f32_e32 v114, 1.0, v114
	v_add_f32_e32 v115, 1.0, v115
	v_exp_f32_e32 v120, v120
	v_exp_f32_e32 v121, v121
	v_mul_f32_e32 v108, 0xbfb8aa3b, v108
	v_mul_f32_e32 v109, 0xbfb8aa3b, v109
	v_add_f32_e32 v102, v102, v134
	v_add_f32_e32 v103, v103, v135
	v_add_f32_e32 v104, v104, v136
	v_exp_f32_e32 v100, v100
	v_add_f32_e32 v105, v105, v137
	v_exp_f32_e32 v101, v101
	v_rcp_f32_e32 v114, v114
	v_rcp_f32_e32 v115, v115
	v_add_f32_e32 v116, 1.0, v116
	v_add_f32_e32 v117, 1.0, v117
	v_exp_f32_e32 v108, v108
	v_exp_f32_e32 v109, v109
	v_mul_f32_e32 v102, 0xbfb8aa3b, v102
	v_mul_f32_e32 v103, 0xbfb8aa3b, v103
	v_mul_f32_e32 v104, 0xbfb8aa3b, v104
	v_mul_f32_e32 v105, 0xbfb8aa3b, v105
	v_rcp_f32_e32 v116, v116
	v_rcp_f32_e32 v117, v117
	v_add_f32_e32 v110, 1.0, v110
	v_add_f32_e32 v111, 1.0, v111
	v_exp_f32_e32 v102, v102
	v_exp_f32_e32 v103, v103
	v_exp_f32_e32 v104, v104
	v_exp_f32_e32 v105, v105
	v_rcp_f32_e32 v110, v110
	v_rcp_f32_e32 v106, v106
	v_rcp_f32_e32 v107, v107
	v_rcp_f32_e32 v111, v111
	v_add_f32_e32 v98, 1.0, v98
	v_add_f32_e32 v99, 1.0, v99
	v_add_f32_e32 v120, 1.0, v120
	v_add_f32_e32 v121, 1.0, v121
	v_lshlrev_b32_e32 v128, 16, v206
	v_and_b32_e32 v129, 0xffff0000, v206
	v_rcp_f32_e32 v98, v98
	v_rcp_f32_e32 v99, v99
	v_add_f32_e32 v100, 1.0, v100
	v_add_f32_e32 v101, 1.0, v101
	v_rcp_f32_e32 v120, v120
	v_rcp_f32_e32 v121, v121
	v_lshlrev_b32_e32 v203, 16, v207
	v_and_b32_e32 v204, 0xffff0000, v207
	v_mul_f32_e32 v114, v114, v128
	v_mul_f32_e32 v115, v115, v129
	v_add_f32_e32 v108, 1.0, v108
	v_add_f32_e32 v109, 1.0, v109
	v_rcp_f32_e32 v100, v100
	v_rcp_f32_e32 v101, v101
	v_cvt_pk_bf16_f32 v128, v114, v115
	v_mul_f32_e32 v114, v116, v203
	v_mul_f32_e32 v115, v117, v204
	v_rcp_f32_e32 v108, v108
	v_rcp_f32_e32 v109, v109
	s_waitcnt vmcnt(6)
	v_lshlrev_b32_e32 v113, 16, v170
	v_and_b32_e32 v119, 0xffff0000, v170
	v_add_f32_e32 v102, 1.0, v102
	v_add_f32_e32 v103, 1.0, v103
	v_add_f32_e32 v104, 1.0, v104
	v_add_f32_e32 v105, 1.0, v105
	v_cvt_pk_bf16_f32 v129, v114, v115
	v_lshlrev_b64 v[114:115], 11, v[214:215]
	v_cvt_pk_bf16_f32 v106, v110, v106
	v_cvt_pk_bf16_f32 v107, v107, v111
	v_mul_f32_e32 v110, v118, v113
	v_mul_f32_e32 v111, v112, v119
	v_rcp_f32_e32 v102, v102
	v_rcp_f32_e32 v103, v103
	v_rcp_f32_e32 v104, v104
	v_rcp_f32_e32 v105, v105
	v_lshlrev_b32_e32 v112, 16, v172
	v_and_b32_e32 v113, 0xffff0000, v172
	v_add_f32_e32 v90, v90, v142
	v_lshl_add_u64 v[116:117], s[16:17], 0, v[114:115]
	v_lshlrev_b32_e32 v118, 16, v173
	v_and_b32_e32 v119, 0xffff0000, v173
	v_mul_f32_e32 v98, v98, v112
	v_mul_f32_e32 v99, v99, v113
	v_mul_f32_e32 v90, 0xbfb8aa3b, v90
	v_add_f32_e32 v95, v95, v147
	v_cvt_pk_bf16_f32 v125, v120, v121
	v_lshl_add_u64 v[116:117], v[116:117], 0, v[208:209]
	v_lshl_add_u64 v[114:115], s[18:19], 0, v[114:115]
	v_lshlrev_b32_e32 v120, 16, v171
	v_and_b32_e32 v121, 0xffff0000, v171
	v_cvt_pk_bf16_f32 v112, v98, v99
	v_mul_f32_e32 v98, v100, v118
	v_mul_f32_e32 v99, v101, v119
	v_exp_f32_e32 v90, v90
	v_mul_f32_e32 v95, 0xbfb8aa3b, v95
	v_lshl_add_u64 v[114:115], v[114:115], 0, v[208:209]
	v_mul_f32_e32 v108, v108, v120
	v_mul_f32_e32 v109, v109, v121
	v_cvt_pk_bf16_f32 v113, v98, v99
	v_add_co_u32_e32 v98, vcc, s65, v116
	v_exp_f32_e32 v95, v95
	global_store_dwordx4 v[116:117], v[122:125], off
	global_store_dwordx4 v[114:115], v[126:129], off
	v_cvt_pk_bf16_f32 v110, v110, v111
	v_cvt_pk_bf16_f32 v111, v108, v109
	v_cvt_pk_bf16_f32 v108, v102, v103
	v_cvt_pk_bf16_f32 v109, v104, v105
	v_addc_co_u32_e32 v99, vcc, 0, v117, vcc
	global_store_dwordx4 v[98:99], v[106:109], off
	v_add_co_u32_e32 v98, vcc, s65, v114
	v_add_f32_e32 v90, 1.0, v90
	s_nop 0
	v_addc_co_u32_e32 v99, vcc, 0, v115, vcc
	v_add_f32_e32 v91, v91, v143
	global_store_dwordx4 v[98:99], v[110:113], off
	v_mul_f32_e32 v91, 0xbfb8aa3b, v91
	v_rcp_f32_e32 v98, v90
	v_add_f32_e32 v90, 1.0, v95
	v_add_f32_e32 v95, v96, v148
	v_exp_f32_e32 v91, v91
	v_mul_f32_e32 v95, 0xbfb8aa3b, v95
	v_exp_f32_e32 v95, v95
	v_add_f32_e32 v94, v94, v146
	v_add_f32_e32 v91, 1.0, v91
	v_rcp_f32_e32 v96, v91
	v_add_f32_e32 v91, 1.0, v95
	v_add_f32_e32 v95, v97, v149
	v_mul_f32_e32 v94, 0xbfb8aa3b, v94
	v_mul_f32_e32 v95, 0xbfb8aa3b, v95
	v_add_f32_e32 v82, v82, v130
	v_add_f32_e32 v83, v83, v131
	v_exp_f32_e32 v94, v94
	v_exp_f32_e32 v95, v95
	v_mul_f32_e32 v82, 0xbfb8aa3b, v82
	v_mul_f32_e32 v83, 0xbfb8aa3b, v83
	v_add_f32_e32 v84, v84, v132
	v_add_f32_e32 v85, v85, v133
	v_add_f32_e32 v92, v92, v144
	v_add_f32_e32 v93, v93, v145
	v_exp_f32_e32 v82, v82
	v_exp_f32_e32 v83, v83
	v_mul_f32_e32 v84, 0xbfb8aa3b, v84
	v_mul_f32_e32 v85, 0xbfb8aa3b, v85
	v_mul_f32_e32 v92, 0xbfb8aa3b, v92
	v_mul_f32_e32 v93, 0xbfb8aa3b, v93
	v_add_f32_e32 v86, v86, v134
	v_add_f32_e32 v87, v87, v135
	v_add_f32_e32 v88, v88, v136
	v_exp_f32_e32 v84, v84
	v_add_f32_e32 v89, v89, v137
	v_exp_f32_e32 v85, v85
	v_exp_f32_e32 v92, v92
	v_exp_f32_e32 v93, v93
	v_mul_f32_e32 v86, 0xbfb8aa3b, v86
	v_mul_f32_e32 v87, 0xbfb8aa3b, v87
	v_mul_f32_e32 v88, 0xbfb8aa3b, v88
	v_mul_f32_e32 v89, 0xbfb8aa3b, v89
	v_add_f32_e32 v94, 1.0, v94
	v_add_f32_e32 v95, 1.0, v95
	v_exp_f32_e32 v86, v86
	v_exp_f32_e32 v87, v87
	v_exp_f32_e32 v88, v88
	v_exp_f32_e32 v89, v89
	v_rcp_f32_e32 v94, v94
	v_rcp_f32_e32 v90, v90
	v_rcp_f32_e32 v91, v91
	v_rcp_f32_e32 v95, v95
	v_add_f32_e32 v82, 1.0, v82
	v_add_f32_e32 v83, 1.0, v83
	v_rcp_f32_e32 v82, v82
	v_rcp_f32_e32 v83, v83
	v_add_f32_e32 v84, 1.0, v84
	v_add_f32_e32 v85, 1.0, v85
	v_add_f32_e32 v92, 1.0, v92
	v_add_f32_e32 v93, 1.0, v93
	v_rcp_f32_e32 v84, v84
	v_rcp_f32_e32 v85, v85
	v_rcp_f32_e32 v92, v92
	v_rcp_f32_e32 v93, v93
	s_waitcnt vmcnt(9)
	v_lshlrev_b32_e32 v97, 16, v166
	v_and_b32_e32 v99, 0xffff0000, v166
	v_add_f32_e32 v86, 1.0, v86
	v_add_f32_e32 v87, 1.0, v87
	v_add_f32_e32 v88, 1.0, v88
	v_add_f32_e32 v89, 1.0, v89
	v_cvt_pk_bf16_f32 v90, v94, v90
	v_cvt_pk_bf16_f32 v91, v91, v95
	v_mul_f32_e32 v94, v98, v97
	v_mul_f32_e32 v95, v96, v99
	v_rcp_f32_e32 v86, v86
	v_rcp_f32_e32 v87, v87
	v_rcp_f32_e32 v88, v88
	v_rcp_f32_e32 v89, v89
	v_lshlrev_b32_e32 v96, 16, v168
	v_and_b32_e32 v97, 0xffff0000, v168
	v_add_f32_e32 v74, v74, v142
	v_lshlrev_b32_e32 v98, 16, v169
	v_and_b32_e32 v99, 0xffff0000, v169
	v_mul_f32_e32 v82, v82, v96
	v_mul_f32_e32 v83, v83, v97
	v_mul_f32_e32 v74, 0xbfb8aa3b, v74
	v_add_f32_e32 v79, v79, v147
	v_lshlrev_b32_e32 v100, 16, v167
	v_and_b32_e32 v101, 0xffff0000, v167
	v_cvt_pk_bf16_f32 v96, v82, v83
	v_mul_f32_e32 v82, v84, v98
	v_mul_f32_e32 v83, v85, v99
	v_exp_f32_e32 v74, v74
	v_mul_f32_e32 v79, 0xbfb8aa3b, v79
	v_mul_f32_e32 v92, v92, v100
	v_mul_f32_e32 v93, v93, v101
	v_cvt_pk_bf16_f32 v97, v82, v83
	v_add_co_u32_e32 v82, vcc, s54, v116
	v_exp_f32_e32 v79, v79
	v_cvt_pk_bf16_f32 v94, v94, v95
	v_cvt_pk_bf16_f32 v95, v92, v93
	v_cvt_pk_bf16_f32 v92, v86, v87
	v_cvt_pk_bf16_f32 v93, v88, v89
	v_addc_co_u32_e32 v83, vcc, 0, v117, vcc
	global_store_dwordx4 v[82:83], v[90:93], off
	v_add_co_u32_e32 v82, vcc, s54, v114
	v_add_f32_e32 v74, 1.0, v74
	s_nop 0
	v_addc_co_u32_e32 v83, vcc, 0, v115, vcc
	v_add_f32_e32 v75, v75, v143
	global_store_dwordx4 v[82:83], v[94:97], off
	v_mul_f32_e32 v75, 0xbfb8aa3b, v75
	v_rcp_f32_e32 v82, v74
	v_add_f32_e32 v74, 1.0, v79
	v_add_f32_e32 v79, v80, v148
	v_exp_f32_e32 v75, v75
	v_mul_f32_e32 v79, 0xbfb8aa3b, v79
	v_exp_f32_e32 v79, v79
	v_add_f32_e32 v78, v78, v146
	v_add_f32_e32 v75, 1.0, v75
	v_rcp_f32_e32 v80, v75
	v_add_f32_e32 v75, 1.0, v79
	v_add_f32_e32 v79, v81, v149
	v_mul_f32_e32 v78, 0xbfb8aa3b, v78
	v_mul_f32_e32 v79, 0xbfb8aa3b, v79
	v_add_f32_e32 v66, v66, v130
	v_add_f32_e32 v67, v67, v131
	v_exp_f32_e32 v78, v78
	v_exp_f32_e32 v79, v79
	v_mul_f32_e32 v66, 0xbfb8aa3b, v66
	v_mul_f32_e32 v67, 0xbfb8aa3b, v67
	v_add_f32_e32 v68, v68, v132
	v_add_f32_e32 v69, v69, v133
	v_add_f32_e32 v76, v76, v144
	v_add_f32_e32 v77, v77, v145
	v_exp_f32_e32 v66, v66
	v_exp_f32_e32 v67, v67
	v_mul_f32_e32 v68, 0xbfb8aa3b, v68
	v_mul_f32_e32 v69, 0xbfb8aa3b, v69
	v_mul_f32_e32 v76, 0xbfb8aa3b, v76
	v_mul_f32_e32 v77, 0xbfb8aa3b, v77
	v_add_f32_e32 v70, v70, v134
	v_add_f32_e32 v71, v71, v135
	v_add_f32_e32 v72, v72, v136
	v_exp_f32_e32 v68, v68
	v_add_f32_e32 v73, v73, v137
	v_exp_f32_e32 v69, v69
	v_exp_f32_e32 v76, v76
	v_exp_f32_e32 v77, v77
	v_mul_f32_e32 v70, 0xbfb8aa3b, v70
	v_mul_f32_e32 v71, 0xbfb8aa3b, v71
	v_mul_f32_e32 v72, 0xbfb8aa3b, v72
	v_mul_f32_e32 v73, 0xbfb8aa3b, v73
	v_add_f32_e32 v78, 1.0, v78
	v_add_f32_e32 v79, 1.0, v79
	v_exp_f32_e32 v70, v70
	v_exp_f32_e32 v71, v71
	v_exp_f32_e32 v72, v72
	v_exp_f32_e32 v73, v73
	v_rcp_f32_e32 v78, v78
	v_rcp_f32_e32 v74, v74
	v_rcp_f32_e32 v75, v75
	v_rcp_f32_e32 v79, v79
	v_add_f32_e32 v66, 1.0, v66
	v_add_f32_e32 v67, 1.0, v67
	v_rcp_f32_e32 v66, v66
	v_rcp_f32_e32 v67, v67
	v_add_f32_e32 v68, 1.0, v68
	v_add_f32_e32 v69, 1.0, v69
	v_add_f32_e32 v76, 1.0, v76
	v_add_f32_e32 v77, 1.0, v77
	v_rcp_f32_e32 v68, v68
	v_rcp_f32_e32 v69, v69
	v_rcp_f32_e32 v76, v76
	v_rcp_f32_e32 v77, v77
	s_waitcnt vmcnt(10)
	v_lshlrev_b32_e32 v81, 16, v162
	v_and_b32_e32 v83, 0xffff0000, v162
	v_add_f32_e32 v70, 1.0, v70
	v_add_f32_e32 v71, 1.0, v71
	v_add_f32_e32 v72, 1.0, v72
	v_add_f32_e32 v73, 1.0, v73
	v_cvt_pk_bf16_f32 v74, v78, v74
	v_cvt_pk_bf16_f32 v75, v75, v79
	v_mul_f32_e32 v78, v82, v81
	v_mul_f32_e32 v79, v80, v83
	v_rcp_f32_e32 v70, v70
	v_rcp_f32_e32 v71, v71
	v_rcp_f32_e32 v72, v72
	v_rcp_f32_e32 v73, v73
	v_lshlrev_b32_e32 v80, 16, v164
	v_and_b32_e32 v81, 0xffff0000, v164
	v_add_f32_e32 v58, v58, v142
	v_lshlrev_b32_e32 v82, 16, v165
	v_and_b32_e32 v83, 0xffff0000, v165
	v_mul_f32_e32 v66, v66, v80
	v_mul_f32_e32 v67, v67, v81
	v_mul_f32_e32 v58, 0xbfb8aa3b, v58
	v_add_f32_e32 v63, v63, v147
	v_lshlrev_b32_e32 v84, 16, v163
	v_and_b32_e32 v85, 0xffff0000, v163
	v_cvt_pk_bf16_f32 v80, v66, v67
	v_mul_f32_e32 v66, v68, v82
	v_mul_f32_e32 v67, v69, v83
	v_exp_f32_e32 v58, v58
	v_mul_f32_e32 v63, 0xbfb8aa3b, v63
	v_mul_f32_e32 v76, v76, v84
	v_mul_f32_e32 v77, v77, v85
	v_cvt_pk_bf16_f32 v81, v66, v67
	v_add_co_u32_e32 v66, vcc, s64, v116
	v_exp_f32_e32 v63, v63
	v_cvt_pk_bf16_f32 v78, v78, v79
	v_cvt_pk_bf16_f32 v79, v76, v77
	v_cvt_pk_bf16_f32 v76, v70, v71
	v_cvt_pk_bf16_f32 v77, v72, v73
	v_addc_co_u32_e32 v67, vcc, 0, v117, vcc
	global_store_dwordx4 v[66:67], v[74:77], off
	v_add_co_u32_e32 v66, vcc, s64, v114
	v_add_f32_e32 v58, 1.0, v58
	s_nop 0
	v_addc_co_u32_e32 v67, vcc, 0, v115, vcc
	v_add_f32_e32 v59, v59, v143
	global_store_dwordx4 v[66:67], v[78:81], off
	v_mul_f32_e32 v59, 0xbfb8aa3b, v59
	v_rcp_f32_e32 v66, v58
	v_add_f32_e32 v58, 1.0, v63
	v_add_f32_e32 v63, v64, v148
	v_exp_f32_e32 v59, v59
	v_mul_f32_e32 v63, 0xbfb8aa3b, v63
	v_exp_f32_e32 v63, v63
	v_add_f32_e32 v62, v62, v146
	v_add_f32_e32 v59, 1.0, v59
	v_rcp_f32_e32 v64, v59
	v_add_f32_e32 v59, 1.0, v63
	v_add_f32_e32 v63, v65, v149
	v_mul_f32_e32 v62, 0xbfb8aa3b, v62
	v_mul_f32_e32 v63, 0xbfb8aa3b, v63
	v_add_f32_e32 v50, v50, v130
	v_add_f32_e32 v51, v51, v131
	v_exp_f32_e32 v62, v62
	v_exp_f32_e32 v63, v63
	v_mul_f32_e32 v50, 0xbfb8aa3b, v50
	v_mul_f32_e32 v51, 0xbfb8aa3b, v51
	v_add_f32_e32 v52, v52, v132
	v_add_f32_e32 v53, v53, v133
	v_add_f32_e32 v60, v60, v144
	v_add_f32_e32 v61, v61, v145
	v_exp_f32_e32 v50, v50
	v_exp_f32_e32 v51, v51
	v_mul_f32_e32 v52, 0xbfb8aa3b, v52
	v_mul_f32_e32 v53, 0xbfb8aa3b, v53
	v_mul_f32_e32 v60, 0xbfb8aa3b, v60
	v_mul_f32_e32 v61, 0xbfb8aa3b, v61
	v_add_f32_e32 v54, v54, v134
	v_add_f32_e32 v55, v55, v135
	v_add_f32_e32 v56, v56, v136
	v_exp_f32_e32 v52, v52
	v_add_f32_e32 v57, v57, v137
	v_exp_f32_e32 v53, v53
	v_exp_f32_e32 v60, v60
	v_exp_f32_e32 v61, v61
	v_mul_f32_e32 v54, 0xbfb8aa3b, v54
	v_mul_f32_e32 v55, 0xbfb8aa3b, v55
	v_mul_f32_e32 v56, 0xbfb8aa3b, v56
	v_mul_f32_e32 v57, 0xbfb8aa3b, v57
	v_add_f32_e32 v62, 1.0, v62
	v_add_f32_e32 v63, 1.0, v63
	v_exp_f32_e32 v54, v54
	v_exp_f32_e32 v55, v55
	v_exp_f32_e32 v56, v56
	v_exp_f32_e32 v57, v57
	v_rcp_f32_e32 v62, v62
	v_rcp_f32_e32 v58, v58
	v_rcp_f32_e32 v59, v59
	v_rcp_f32_e32 v63, v63
	v_add_f32_e32 v50, 1.0, v50
	v_add_f32_e32 v51, 1.0, v51
	v_rcp_f32_e32 v50, v50
	v_rcp_f32_e32 v51, v51
	v_add_f32_e32 v52, 1.0, v52
	v_add_f32_e32 v53, 1.0, v53
	v_add_f32_e32 v60, 1.0, v60
	v_add_f32_e32 v61, 1.0, v61
	v_rcp_f32_e32 v52, v52
	v_rcp_f32_e32 v53, v53
	v_rcp_f32_e32 v60, v60
	v_rcp_f32_e32 v61, v61
	s_waitcnt vmcnt(11)
	v_lshlrev_b32_e32 v65, 16, v158
	v_and_b32_e32 v67, 0xffff0000, v158
	v_add_f32_e32 v54, 1.0, v54
	v_add_f32_e32 v55, 1.0, v55
	v_add_f32_e32 v56, 1.0, v56
	v_add_f32_e32 v57, 1.0, v57
	v_cvt_pk_bf16_f32 v58, v62, v58
	v_cvt_pk_bf16_f32 v59, v59, v63
	v_mul_f32_e32 v62, v66, v65
	v_mul_f32_e32 v63, v64, v67
	v_rcp_f32_e32 v54, v54
	v_rcp_f32_e32 v55, v55
	v_rcp_f32_e32 v56, v56
	v_rcp_f32_e32 v57, v57
	v_lshlrev_b32_e32 v64, 16, v160
	v_and_b32_e32 v65, 0xffff0000, v160
	v_add_f32_e32 v42, v42, v142
	v_lshlrev_b32_e32 v66, 16, v161
	v_and_b32_e32 v67, 0xffff0000, v161
	v_mul_f32_e32 v50, v50, v64
	v_mul_f32_e32 v51, v51, v65
	v_mul_f32_e32 v42, 0xbfb8aa3b, v42
	v_add_f32_e32 v47, v47, v147
	v_lshlrev_b32_e32 v68, 16, v159
	v_and_b32_e32 v69, 0xffff0000, v159
	v_cvt_pk_bf16_f32 v64, v50, v51
	v_mul_f32_e32 v50, v52, v66
	v_mul_f32_e32 v51, v53, v67
	v_exp_f32_e32 v42, v42
	v_mul_f32_e32 v47, 0xbfb8aa3b, v47
	v_mul_f32_e32 v60, v60, v68
	v_mul_f32_e32 v61, v61, v69
	v_cvt_pk_bf16_f32 v65, v50, v51
	v_add_co_u32_e32 v50, vcc, s69, v116
	v_exp_f32_e32 v47, v47
	v_cvt_pk_bf16_f32 v62, v62, v63
	v_cvt_pk_bf16_f32 v63, v60, v61
	v_cvt_pk_bf16_f32 v60, v54, v55
	v_cvt_pk_bf16_f32 v61, v56, v57
	v_addc_co_u32_e32 v51, vcc, 0, v117, vcc
	global_store_dwordx4 v[50:51], v[58:61], off
	v_add_co_u32_e32 v50, vcc, s69, v114
	v_add_f32_e32 v42, 1.0, v42
	s_nop 0
	v_addc_co_u32_e32 v51, vcc, 0, v115, vcc
	v_add_f32_e32 v43, v43, v143
	global_store_dwordx4 v[50:51], v[62:65], off
	v_mul_f32_e32 v43, 0xbfb8aa3b, v43
	v_rcp_f32_e32 v50, v42
	v_add_f32_e32 v42, 1.0, v47
	v_add_f32_e32 v47, v48, v148
	v_exp_f32_e32 v43, v43
	v_mul_f32_e32 v47, 0xbfb8aa3b, v47
	v_exp_f32_e32 v47, v47
	v_add_f32_e32 v46, v46, v146
	v_add_f32_e32 v43, 1.0, v43
	v_rcp_f32_e32 v48, v43
	v_add_f32_e32 v43, 1.0, v47
	v_add_f32_e32 v47, v49, v149
	v_mul_f32_e32 v46, 0xbfb8aa3b, v46
	v_mul_f32_e32 v47, 0xbfb8aa3b, v47
	v_add_f32_e32 v34, v34, v130
	v_add_f32_e32 v35, v35, v131
	v_exp_f32_e32 v46, v46
	v_exp_f32_e32 v47, v47
	v_mul_f32_e32 v34, 0xbfb8aa3b, v34
	v_mul_f32_e32 v35, 0xbfb8aa3b, v35
	v_add_f32_e32 v36, v36, v132
	v_add_f32_e32 v37, v37, v133
	v_add_f32_e32 v44, v44, v144
	v_add_f32_e32 v45, v45, v145
	v_exp_f32_e32 v34, v34
	v_exp_f32_e32 v35, v35
	v_mul_f32_e32 v36, 0xbfb8aa3b, v36
	v_mul_f32_e32 v37, 0xbfb8aa3b, v37
	v_mul_f32_e32 v44, 0xbfb8aa3b, v44
	v_mul_f32_e32 v45, 0xbfb8aa3b, v45
	v_add_f32_e32 v38, v38, v134
	v_add_f32_e32 v39, v39, v135
	v_add_f32_e32 v40, v40, v136
	v_exp_f32_e32 v36, v36
	v_add_f32_e32 v41, v41, v137
	v_exp_f32_e32 v37, v37
	v_exp_f32_e32 v44, v44
	v_exp_f32_e32 v45, v45
	v_mul_f32_e32 v38, 0xbfb8aa3b, v38
	v_mul_f32_e32 v39, 0xbfb8aa3b, v39
	v_mul_f32_e32 v40, 0xbfb8aa3b, v40
	v_mul_f32_e32 v41, 0xbfb8aa3b, v41
	v_add_f32_e32 v46, 1.0, v46
	v_add_f32_e32 v47, 1.0, v47
	v_exp_f32_e32 v38, v38
	v_exp_f32_e32 v39, v39
	v_exp_f32_e32 v40, v40
	v_exp_f32_e32 v41, v41
	v_rcp_f32_e32 v46, v46
	v_rcp_f32_e32 v42, v42
	v_rcp_f32_e32 v43, v43
	v_rcp_f32_e32 v47, v47
	v_add_f32_e32 v34, 1.0, v34
	v_add_f32_e32 v35, 1.0, v35
	v_rcp_f32_e32 v34, v34
	v_rcp_f32_e32 v35, v35
	v_add_f32_e32 v36, 1.0, v36
	v_add_f32_e32 v37, 1.0, v37
	v_add_f32_e32 v44, 1.0, v44
	v_add_f32_e32 v45, 1.0, v45
	v_rcp_f32_e32 v36, v36
	v_rcp_f32_e32 v37, v37
	v_rcp_f32_e32 v44, v44
	v_rcp_f32_e32 v45, v45
	s_waitcnt vmcnt(12)
	v_lshlrev_b32_e32 v49, 16, v154
	v_and_b32_e32 v51, 0xffff0000, v154
	v_add_f32_e32 v38, 1.0, v38
	v_add_f32_e32 v39, 1.0, v39
	v_add_f32_e32 v40, 1.0, v40
	v_add_f32_e32 v41, 1.0, v41
	v_cvt_pk_bf16_f32 v42, v46, v42
	v_cvt_pk_bf16_f32 v43, v43, v47
	v_mul_f32_e32 v46, v50, v49
	v_mul_f32_e32 v47, v48, v51
	v_rcp_f32_e32 v38, v38
	v_rcp_f32_e32 v39, v39
	v_rcp_f32_e32 v40, v40
	v_rcp_f32_e32 v41, v41
	v_lshlrev_b32_e32 v48, 16, v156
	v_and_b32_e32 v49, 0xffff0000, v156
	v_add_f32_e32 v26, v26, v142
	v_lshlrev_b32_e32 v50, 16, v157
	v_and_b32_e32 v51, 0xffff0000, v157
	v_mul_f32_e32 v34, v34, v48
	v_mul_f32_e32 v35, v35, v49
	v_mul_f32_e32 v26, 0xbfb8aa3b, v26
	v_add_f32_e32 v31, v31, v147
	v_lshlrev_b32_e32 v52, 16, v155
	v_and_b32_e32 v53, 0xffff0000, v155
	v_cvt_pk_bf16_f32 v48, v34, v35
	v_mul_f32_e32 v34, v36, v50
	v_mul_f32_e32 v35, v37, v51
	v_exp_f32_e32 v26, v26
	v_mul_f32_e32 v31, 0xbfb8aa3b, v31
	v_mul_f32_e32 v44, v44, v52
	v_mul_f32_e32 v45, v45, v53
	v_cvt_pk_bf16_f32 v49, v34, v35
	v_add_co_u32_e32 v34, vcc, s70, v116
	v_exp_f32_e32 v31, v31
	v_cvt_pk_bf16_f32 v46, v46, v47
	v_cvt_pk_bf16_f32 v47, v44, v45
	v_cvt_pk_bf16_f32 v44, v38, v39
	v_cvt_pk_bf16_f32 v45, v40, v41
	v_addc_co_u32_e32 v35, vcc, 0, v117, vcc
	global_store_dwordx4 v[34:35], v[42:45], off
	v_add_co_u32_e32 v34, vcc, s70, v114
	v_add_f32_e32 v26, 1.0, v26
	s_nop 0
	v_addc_co_u32_e32 v35, vcc, 0, v115, vcc
	v_add_f32_e32 v27, v27, v143
	global_store_dwordx4 v[34:35], v[46:49], off
	v_mul_f32_e32 v27, 0xbfb8aa3b, v27
	v_rcp_f32_e32 v34, v26
	v_add_f32_e32 v26, 1.0, v31
	v_add_f32_e32 v31, v32, v148
	v_exp_f32_e32 v27, v27
	v_mul_f32_e32 v31, 0xbfb8aa3b, v31
	v_exp_f32_e32 v31, v31
	v_add_f32_e32 v30, v30, v146
	v_add_f32_e32 v27, 1.0, v27
	v_rcp_f32_e32 v32, v27
	v_add_f32_e32 v27, 1.0, v31
	v_add_f32_e32 v31, v33, v149
	v_mul_f32_e32 v30, 0xbfb8aa3b, v30
	v_mul_f32_e32 v31, 0xbfb8aa3b, v31
	v_add_f32_e32 v18, v18, v130
	v_add_f32_e32 v19, v19, v131
	v_exp_f32_e32 v30, v30
	v_exp_f32_e32 v31, v31
	v_mul_f32_e32 v18, 0xbfb8aa3b, v18
	v_mul_f32_e32 v19, 0xbfb8aa3b, v19
	v_add_f32_e32 v20, v20, v132
	v_add_f32_e32 v21, v21, v133
	v_add_f32_e32 v28, v28, v144
	v_add_f32_e32 v29, v29, v145
	v_exp_f32_e32 v18, v18
	v_exp_f32_e32 v19, v19
	v_mul_f32_e32 v20, 0xbfb8aa3b, v20
	v_mul_f32_e32 v21, 0xbfb8aa3b, v21
	v_mul_f32_e32 v28, 0xbfb8aa3b, v28
	v_mul_f32_e32 v29, 0xbfb8aa3b, v29
	v_add_f32_e32 v22, v22, v134
	v_add_f32_e32 v23, v23, v135
	v_add_f32_e32 v24, v24, v136
	v_exp_f32_e32 v20, v20
	v_add_f32_e32 v25, v25, v137
	v_exp_f32_e32 v21, v21
	v_exp_f32_e32 v28, v28
	v_exp_f32_e32 v29, v29
	v_mul_f32_e32 v22, 0xbfb8aa3b, v22
	v_mul_f32_e32 v23, 0xbfb8aa3b, v23
	v_mul_f32_e32 v24, 0xbfb8aa3b, v24
	v_mul_f32_e32 v25, 0xbfb8aa3b, v25
	v_add_f32_e32 v30, 1.0, v30
	v_add_f32_e32 v31, 1.0, v31
	v_exp_f32_e32 v22, v22
	v_exp_f32_e32 v23, v23
	v_exp_f32_e32 v24, v24
	v_exp_f32_e32 v25, v25
	v_rcp_f32_e32 v30, v30
	v_rcp_f32_e32 v26, v26
	v_rcp_f32_e32 v27, v27
	v_rcp_f32_e32 v31, v31
	v_add_f32_e32 v18, 1.0, v18
	v_add_f32_e32 v19, 1.0, v19
	v_rcp_f32_e32 v18, v18
	v_rcp_f32_e32 v19, v19
	v_add_f32_e32 v20, 1.0, v20
	v_add_f32_e32 v21, 1.0, v21
	v_add_f32_e32 v28, 1.0, v28
	v_add_f32_e32 v29, 1.0, v29
	v_rcp_f32_e32 v20, v20
	v_rcp_f32_e32 v21, v21
	v_rcp_f32_e32 v28, v28
	v_rcp_f32_e32 v29, v29
	s_waitcnt vmcnt(13)
	v_lshlrev_b32_e32 v33, 16, v150
	v_and_b32_e32 v35, 0xffff0000, v150
	v_add_f32_e32 v22, 1.0, v22
	v_add_f32_e32 v23, 1.0, v23
	v_add_f32_e32 v24, 1.0, v24
	v_add_f32_e32 v25, 1.0, v25
	v_cvt_pk_bf16_f32 v26, v30, v26
	v_cvt_pk_bf16_f32 v27, v27, v31
	v_mul_f32_e32 v30, v34, v33
	v_mul_f32_e32 v31, v32, v35
	v_rcp_f32_e32 v22, v22
	v_rcp_f32_e32 v23, v23
	v_rcp_f32_e32 v24, v24
	v_rcp_f32_e32 v25, v25
	v_lshlrev_b32_e32 v32, 16, v152
	v_and_b32_e32 v33, 0xffff0000, v152
	v_add_f32_e32 v10, v10, v142
	v_lshlrev_b32_e32 v34, 16, v153
	v_and_b32_e32 v35, 0xffff0000, v153
	v_mul_f32_e32 v18, v18, v32
	v_mul_f32_e32 v19, v19, v33
	v_mul_f32_e32 v10, 0xbfb8aa3b, v10
	v_add_f32_e32 v15, v15, v147
	v_lshlrev_b32_e32 v36, 16, v151
	v_and_b32_e32 v37, 0xffff0000, v151
	v_cvt_pk_bf16_f32 v32, v18, v19
	v_mul_f32_e32 v18, v20, v34
	v_mul_f32_e32 v19, v21, v35
	v_exp_f32_e32 v10, v10
	v_mul_f32_e32 v15, 0xbfb8aa3b, v15
	v_mul_f32_e32 v28, v28, v36
	v_mul_f32_e32 v29, v29, v37
	v_cvt_pk_bf16_f32 v33, v18, v19
	v_add_co_u32_e32 v18, vcc, s71, v116
	v_exp_f32_e32 v15, v15
	v_cvt_pk_bf16_f32 v30, v30, v31
	v_cvt_pk_bf16_f32 v31, v28, v29
	v_cvt_pk_bf16_f32 v28, v22, v23
	v_cvt_pk_bf16_f32 v29, v24, v25
	v_addc_co_u32_e32 v19, vcc, 0, v117, vcc
	global_store_dwordx4 v[18:19], v[26:29], off
	v_add_co_u32_e32 v18, vcc, s71, v114
	v_add_f32_e32 v10, 1.0, v10
	s_nop 0
	v_addc_co_u32_e32 v19, vcc, 0, v115, vcc
	v_add_f32_e32 v11, v11, v143
	global_store_dwordx4 v[18:19], v[30:33], off
	v_mul_f32_e32 v11, 0xbfb8aa3b, v11
	v_rcp_f32_e32 v18, v10
	v_add_f32_e32 v10, 1.0, v15
	v_add_f32_e32 v15, v16, v148
	v_exp_f32_e32 v11, v11
	v_mul_f32_e32 v15, 0xbfb8aa3b, v15
	v_exp_f32_e32 v15, v15
	v_add_f32_e32 v14, v14, v146
	v_add_f32_e32 v11, 1.0, v11
	v_rcp_f32_e32 v16, v11
	v_add_f32_e32 v11, 1.0, v15
	v_add_f32_e32 v15, v17, v149
	v_mul_f32_e32 v14, 0xbfb8aa3b, v14
	v_mul_f32_e32 v15, 0xbfb8aa3b, v15
	v_add_f32_e32 v2, v2, v130
	v_add_f32_e32 v3, v3, v131
	v_exp_f32_e32 v14, v14
	v_exp_f32_e32 v15, v15
	v_mul_f32_e32 v2, 0xbfb8aa3b, v2
	v_mul_f32_e32 v3, 0xbfb8aa3b, v3
	v_add_f32_e32 v4, v4, v132
	v_add_f32_e32 v5, v5, v133
	v_add_f32_e32 v12, v12, v144
	v_add_f32_e32 v13, v13, v145
	v_exp_f32_e32 v2, v2
	v_exp_f32_e32 v3, v3
	v_mul_f32_e32 v4, 0xbfb8aa3b, v4
	v_mul_f32_e32 v5, 0xbfb8aa3b, v5
	v_mul_f32_e32 v12, 0xbfb8aa3b, v12
	v_mul_f32_e32 v13, 0xbfb8aa3b, v13
	v_add_f32_e32 v6, v6, v134
	v_add_f32_e32 v7, v7, v135
	v_add_f32_e32 v8, v8, v136
	v_exp_f32_e32 v4, v4
	v_add_f32_e32 v9, v9, v137
	v_exp_f32_e32 v5, v5
	v_exp_f32_e32 v12, v12
	v_exp_f32_e32 v13, v13
	v_mul_f32_e32 v6, 0xbfb8aa3b, v6
	v_mul_f32_e32 v7, 0xbfb8aa3b, v7
	v_mul_f32_e32 v8, 0xbfb8aa3b, v8
	v_mul_f32_e32 v9, 0xbfb8aa3b, v9
	v_add_f32_e32 v14, 1.0, v14
	v_add_f32_e32 v15, 1.0, v15
	v_exp_f32_e32 v6, v6
	v_exp_f32_e32 v7, v7
	v_exp_f32_e32 v8, v8
	v_exp_f32_e32 v9, v9
	v_rcp_f32_e32 v14, v14
	v_rcp_f32_e32 v10, v10
	v_rcp_f32_e32 v11, v11
	v_rcp_f32_e32 v15, v15
	v_add_f32_e32 v2, 1.0, v2
	v_add_f32_e32 v3, 1.0, v3
	v_rcp_f32_e32 v2, v2
	v_rcp_f32_e32 v3, v3
	v_add_f32_e32 v4, 1.0, v4
	v_add_f32_e32 v5, 1.0, v5
	v_add_f32_e32 v12, 1.0, v12
	v_add_f32_e32 v13, 1.0, v13
	v_rcp_f32_e32 v4, v4
	v_rcp_f32_e32 v5, v5
	v_rcp_f32_e32 v12, v12
	v_rcp_f32_e32 v13, v13
	s_waitcnt vmcnt(14)
	v_lshlrev_b32_e32 v17, 16, v138
	v_and_b32_e32 v19, 0xffff0000, v138
	v_add_f32_e32 v6, 1.0, v6
	v_add_f32_e32 v7, 1.0, v7
	v_add_f32_e32 v8, 1.0, v8
	v_add_f32_e32 v9, 1.0, v9
	v_cvt_pk_bf16_f32 v10, v14, v10
	v_cvt_pk_bf16_f32 v11, v11, v15
	v_mul_f32_e32 v14, v18, v17
	v_mul_f32_e32 v15, v16, v19
	v_rcp_f32_e32 v6, v6
	v_rcp_f32_e32 v7, v7
	v_rcp_f32_e32 v8, v8
	v_rcp_f32_e32 v9, v9
	v_lshlrev_b32_e32 v16, 16, v140
	v_and_b32_e32 v17, 0xffff0000, v140
	v_lshlrev_b32_e32 v18, 16, v141
	v_and_b32_e32 v19, 0xffff0000, v141
	v_mul_f32_e32 v2, v2, v16
	v_mul_f32_e32 v3, v3, v17
	v_lshlrev_b32_e32 v20, 16, v139
	v_and_b32_e32 v21, 0xffff0000, v139
	v_cvt_pk_bf16_f32 v16, v2, v3
	v_mul_f32_e32 v2, v4, v18
	v_mul_f32_e32 v3, v5, v19
	v_mul_f32_e32 v12, v12, v20
	v_mul_f32_e32 v13, v13, v21
	v_cvt_pk_bf16_f32 v17, v2, v3
	v_add_co_u32_e32 v2, vcc, 0x58000, v116
	v_cvt_pk_bf16_f32 v14, v14, v15
	v_cvt_pk_bf16_f32 v15, v12, v13
	v_cvt_pk_bf16_f32 v12, v6, v7
	v_cvt_pk_bf16_f32 v13, v8, v9
	v_addc_co_u32_e32 v3, vcc, 0, v117, vcc
	global_store_dwordx4 v[2:3], v[10:13], off
	v_add_co_u32_e32 v2, vcc, 0x58000, v114
	s_nop 1
	v_addc_co_u32_e32 v3, vcc, 0, v115, vcc
	global_store_dwordx4 v[2:3], v[14:17], off
	s_andn2_b64 vcc, exec, s[2:3]
	s_mov_b64 s[2:3], -1
	s_cbranch_vccnz .LBB0_632
	s_andn2_b64 vcc, exec, s[14:15]
	s_cbranch_vccnz .LBB0_631
	s_barrier
	s_branch .LBB0_631
